# W_out GEMM phase: every other workgroup of each XCD starts ~14 us later so one half's HBM-bound residual epilogue overlaps the other half's K loop
# baseline (speedup 1.0000x reference)
; #define GAS __attribute__((address_space(1)))
; #define PHASE_ARGS() CArgsP ap = (CArgsP)__builtin_amdgcn_kernarg_segment_ptr(); asm volatile("" : "+s"(ap))
; #define PHASE_FRAME() Frame F = F0; asm volatile("" : "+s"(F.ws), "+s"(F.ctl), "+s"(F.G), "+s"(F.bid), "+s"(F.lds)); \
;     F.ws = (GAS unsigned char*)(GAS unsigned char*)F.ws; F.ctl = (GAS unsigned*)(GAS unsigned*)F.ctl;     \
;     GAS unsigned char* ws = F.ws; (void)ws
; template <int layer>
; __device__ __forceinline__ void run_layer(const Frame& F0, const XcdBarrier& bar, const int lo, const int hi) {
;     ...
;         if (IN(pb + 6)) { PHASE_FRAME();
;             DenseSched S{(const GAS char*)(ws + WS_MRG), (const GAS char*)(ws + WS_WOUT), D_MODEL, D_MODEL, D_MODEL / 128, T / 256, D_MODEL / 256, F.G, F.bid, 1 << 30, 0};
;             PHASE_ARGS(); EpiResid E{(const GAS bf16_t*)(ws + WS_XB), (GAS bf16_t*)(ws + WS_R)};
;             pg8::gemm_phase<EpiResid, DenseSched, false, true, true>(F.lds, S, E);
.LBB0_1222:
	s_cmp_lt_i32 s54, 7
	s_cselect_b64 s[8:9], -1, 0
	s_and_b64 s[0:1], s[8:9], s[4:5]
	s_andn2_b64 vcc, exec, s[0:1]
	s_cbranch_vccnz .LBB0_1249
	v_readlane_b32 s98, v254, 0
	s_bitcmp1_b32 s98, 3
	s_cbranch_scc0 .Lstg_p6a
	s_sleep 127
	s_sleep 127
	s_sleep 127
	s_sleep 64
.Lstg_p6a:
	s_mov_b32 s20, 0
	s_mov_b64 s[2:3], s[52:53]
	v_readlane_b32 s0, v254, 0
	s_mov_b64 s[4:5], s[52:53]
	s_mov_b32 s1, s95
	s_waitcnt vmcnt(13)
	v_mov_b32_e32 v10, v0
	v_readlane_b32 s2, v254, 1
	v_readlane_b32 s3, v254, 2
	s_cmpk_gt_i32 s0, 0x1ff
	v_readfirstlane_b32 s18, v10
	s_cbranch_scc1 .LBB0_1249
	s_ashr_i32 s2, s0, 31
	s_lshr_b32 s3, s2, 29
	s_add_i32 s11, s0, s3
	s_and_b32 s3, s11, -8
	s_sub_i32 s3, s0, s3
	s_cmp_gt_i32 s3, -1
	s_cbranch_scc0 .LBB0_1226
	s_lshl_b32 s10, s3, 6
	s_ashr_i32 s6, s11, 3
	s_cbranch_execz .LBB0_1227
	s_branch .LBB0_1228

; #define GAS __attribute__((address_space(1)))
; #define PHASE_ARGS() CArgsP ap = (CArgsP)__builtin_amdgcn_kernarg_segment_ptr(); asm volatile("" : "+s"(ap))
; #define PHASE_FRAME() Frame F = F0; asm volatile("" : "+s"(F.ws), "+s"(F.ctl), "+s"(F.G), "+s"(F.bid), "+s"(F.lds)); \
;     F.ws = (GAS unsigned char*)(GAS unsigned char*)F.ws; F.ctl = (GAS unsigned*)(GAS unsigned*)F.ctl;     \
;     GAS unsigned char* ws = F.ws; (void)ws
; template <int layer>
; __device__ __forceinline__ void run_layer(const Frame& F0, const XcdBarrier& bar, const int lo, const int hi) {
;     ...
;         if (IN(pb + 6)) { PHASE_FRAME();
;             DenseSched S{(const GAS char*)(ws + WS_MRG), (const GAS char*)(ws + WS_WOUT), D_MODEL, D_MODEL, D_MODEL / 128, T / 256, D_MODEL / 256, F.G, F.bid, 1 << 30, 0};
;             PHASE_ARGS(); EpiResid E{(const GAS bf16_t*)(ws + WS_XB), (GAS bf16_t*)(ws + WS_R)};
;             pg8::gemm_phase<EpiResid, DenseSched, false, true, true>(F.lds, S, E);
.LBB0_2787:
	s_cmp_lt_i32 s54, 18
	s_cselect_b64 s[8:9], -1, 0
	s_and_b64 s[0:1], s[8:9], s[4:5]
	s_andn2_b64 vcc, exec, s[0:1]
	s_cbranch_vccnz .LBB0_2814
	v_readlane_b32 s98, v254, 0
	s_bitcmp1_b32 s98, 3
	s_cbranch_scc0 .Lstg_p6b
	s_sleep 127
	s_sleep 127
	s_sleep 127
	s_sleep 64
.Lstg_p6b:
	s_mov_b32 s20, 0
	s_mov_b64 s[2:3], s[52:53]
	v_readlane_b32 s0, v254, 0
	s_mov_b64 s[4:5], s[52:53]
	s_mov_b32 s1, s95
	s_waitcnt vmcnt(0)
	v_mov_b32_e32 v10, v0
	v_readlane_b32 s2, v254, 1
	v_readlane_b32 s3, v254, 2
	s_cmpk_gt_i32 s0, 0x1ff
	v_readfirstlane_b32 s18, v10
	s_cbranch_scc1 .LBB0_2814
	s_ashr_i32 s2, s0, 31
	s_lshr_b32 s3, s2, 29
	s_add_i32 s11, s0, s3
	s_and_b32 s3, s11, -8
	s_sub_i32 s3, s0, s3
	s_cmp_gt_i32 s3, -1
	s_cbranch_scc0 .LBB0_2791
	s_lshl_b32 s10, s3, 6
	s_ashr_i32 s6, s11, 3
	s_cbranch_execz .LBB0_2792
	s_branch .LBB0_2793
